# gate|up epilogue bias vectors loaded at the unit top into VGPRs free through the K loop: no vmcnt drain at the epilogue
# speedup vs baseline: 1.0078x; 1.0078x over previous
; #define PG8_VOFF(dst, U) do { if constexpr (GATHER) { _Pragma("unroll") for (int h = 0; h < 2; ++h) _Pragma("unroll") for (int i = 0; i < 2; ++i) { \
;         const int row = g.rowidx[(U).pm * BM + h * HALF + i * 64 + R0]; dst[h][i] = (unsigned)row * (unsigned)RB + (unsigned)C0 * 2u; } } } while (0)
;     __device__ __forceinline__ void operator()(const f32x4 (&acc)[2][2][4][2], const Unit& u, int wr, int wc, int fr, int fq) const {
;         const int row0 = u.pm * BM + wr * 64 + fr, col = u.pn * 128 + wc * 32 + 8 * fq;
;         const float* bg = bgu + (size_t)u.e * (2 * DFF) + col;
;         const f32x4 g0 = *(const f32x4*)bg, g1 = *(const f32x4*)(bg + 4), u0 = *(const f32x4*)(bg + DFF), u1 = *(const f32x4*)(bg + DFF + 4);
; template <class Epi, bool GATHER, int MODE, bool SPLIT = false>
; __device__ __forceinline__ void gemm_phase(PG8_LAS unsigned char* lds, const Gemm g, const Order& S, const Epi& E) {
;     ...
;         float rs2[2] = {0.f, 0.f};
;         if constexpr (MODE == 2) {
; #pragma unroll
;             for (int a = 0; a < 2; ++a) rs2[a] = g.rowscale[cur.pm * BM + a * HALF + wr * 64 + fq * 16 + fr]; }
;         const bool has_next = S.next(ui + 1, nxt);
;         const char* nB = has_next ? (const char*)g.Bt + (size_t)nxt.e * g.bstride + (size_t)nxt.pn * tstep : cB;
;         const size_t nAr = has_next ? (size_t)nxt.pm * tstep : cAr;
;         if (has_next) { PG8_VOFF(nv, nxt); }
.LBB0_797:
	s_lshl_b32 s1, s10, 8
	v_add_u32_e32 v2, s1, v171
	v_ashrrev_i32_e32 v3, 31, v2
	v_lshl_add_u64 v[4:5], v[2:3], 2, s[14:15]
	v_add_u32_e32 v2, 0x80, v2
	v_ashrrev_i32_e32 v3, 31, v2
	v_lshl_add_u64 v[2:3], v[2:3], 2, s[14:15]
	global_load_dword v165, v[4:5], off
	global_load_dword v188, v[2:3], off
	s_lshl_b32 s99, s0, 7
	v_ashrrev_i32_e32 v149, 31, v164
	v_mov_b32_e32 v148, v164
	v_or_b32_e32 v150, s99, v177
	v_lshlrev_b64 v[148:149], 14, v[148:149]
	v_ashrrev_i32_e32 v151, 31, v150
	v_lshl_add_u64 v[148:149], s[84:85], 0, v[148:149]
	v_lshl_add_u64 v[148:149], v[150:151], 2, v[148:149]
	v_lshl_add_u64 v[150:151], v[148:149], 0, s[24:25]
	global_load_dwordx4 v[236:239], v[148:149], off
	global_load_dwordx4 v[240:243], v[148:149], off offset:16
	global_load_dwordx4 v[244:247], v[150:151], off
	global_load_dwordx2 v[248:249], v[150:151], off offset:16
	global_load_dwordx2 v[252:253], v[150:151], off offset:24
	s_add_i32 s47, s47, 1
	s_mul_i32 s2, s47, s64
	s_mul_hi_u32 s3, s47, s33
	s_add_i32 s3, s3, s2
	s_mul_i32 s2, s47, s33
	s_add_u32 s2, s2, s92
	s_addc_u32 s3, s3, s45
	v_cmp_ge_i64_e32 vcc, s[2:3], v[162:163]
	v_cmp_lt_i64_e64 s[4:5], s[2:3], v[162:163]
	s_cbranch_vccnz .LBB0_799
	s_ashr_i32 s3, s2, 31
	s_lshr_b32 s3, s3, 29
	s_add_i32 s3, s2, s3
	s_ashr_i32 s10, s3, 3
	s_and_b32 s3, s3, -8
	s_sub_i32 s2, s2, s3
	s_cmp_lt_i32 s2, 0
	s_cselect_b32 s3, s46, s44
	s_mul_i32 s2, s3, s2
	s_add_i32 s2, s2, s10
	s_ashr_i32 s3, s2, 31
	s_lshr_b32 s3, s3, 26
	s_add_i32 s3, s2, s3
	s_ashr_i32 s10, s3, 6
	s_lshl_b32 s10, s10, 2
	s_sub_i32 s11, s38, s10
	s_min_i32 s11, s11, 4
	s_abs_i32 s26, s11
	v_cvt_f32_u32_e32 v2, s26
	s_sub_i32 s28, 0, s26
	s_andn2_b32 s3, s3, 63
	s_sub_i32 s2, s2, s3
	v_rcp_iflag_f32_e32 v2, v2
	s_abs_i32 s3, s2
	s_xor_b32 s27, s2, s11
	s_ashr_i32 s27, s27, 31
	v_mul_f32_e32 v2, 0x4f7ffffe, v2
	v_cvt_u32_f32_e32 v2, v2
	s_nop 0
	v_readfirstlane_b32 s29, v2
	s_mul_i32 s28, s28, s29
	s_mul_hi_u32 s28, s29, s28
	s_add_i32 s29, s29, s28
	s_mul_hi_u32 s28, s3, s29
	s_mul_i32 s29, s28, s26
	s_sub_i32 s3, s3, s29
	s_add_i32 s30, s28, 1
	s_sub_i32 s29, s3, s26
	s_cmp_ge_u32 s3, s26
	s_cselect_b32 s28, s30, s28
	s_cselect_b32 s3, s29, s3
	s_add_i32 s29, s28, 1
	s_cmp_ge_u32 s3, s26
	s_cselect_b32 s3, s29, s28
	s_xor_b32 s3, s3, s27
	s_sub_i32 s26, s3, s27
	s_mul_i32 s3, s26, s11
	s_sub_i32 s2, s2, s3
	s_add_i32 s10, s2, s10
	s_ashr_i32 s11, s10, 31
	s_lshl_b64 s[2:3], s[10:11], 2
	s_add_u32 s2, s39, s2
	s_addc_u32 s3, s40, s3
	global_load_dword v230, v166, s[2:3]

;     __device__ __forceinline__ void operator()(const f32x4 (&acc)[2][2][4][2], const Unit& u, int wr, int wc, int fr, int fq) const {
;     ...
;                     const f32x4 gt = acc[ai][0][m][n] * descale + (n ? g1 : g0), up = acc[ai][1][m][n] * descale + (n ? u1 : u0);
; template <class Epi, bool GATHER, int MODE, bool SPLIT = false>
; __device__ __forceinline__ void gemm_phase(PG8_LAS unsigned char* lds, const Gemm g, const Order& S, const Epi& E) {
;     ...
;         if constexpr (MODE != 0) asm volatile("s_nop 15\n\ts_nop 15" ::: "memory");
;         if constexpr (MODE == 2) {
; #pragma unroll
;             for (int a = 0; a < 2; ++a)
; #pragma unroll
;                 for (int m = 0; m < 4; ++m) { const float rs = __builtin_bit_cast(float, __builtin_amdgcn_ds_bpermute((m * 16 + fr) * 4, __builtin_bit_cast(int, rs2[a])));
; #pragma unroll
;                     for (int b = 0; b < 2; ++b)
; #pragma unroll
;                         for (int n = 0; n < 2; ++n) { const v4i_t iv = __builtin_bit_cast(v4i_t, acc[a][b][m][n]); acc[a][b][m][n] = (f32x4){(float)iv[0], (float)iv[1], (float)iv[2], (float)iv[3]} * rs; } }
.LBB0_805:
	s_nop 7
	ds_bpermute_b32 v194, v170, v165
	ds_bpermute_b32 v196, v174, v165
	ds_bpermute_b32 v198, v175, v165
	ds_bpermute_b32 v200, v176, v165
	ds_bpermute_b32 v202, v170, v188
	ds_bpermute_b32 v204, v174, v188
	ds_bpermute_b32 v206, v175, v188
	ds_bpermute_b32 v208, v176, v188
	s_lshl_b32 s0, s0, 7
	s_mov_b32 s98, 0xc01d265f
	v_bitop3_b32 v130, s0, -16, v177 bitop3:0xc8
	v_add_u32_e32 v232, s1, v169
	v_ashrrev_i32_e32 v131, 31, v130
	v_add_u32_e32 v233, 0x80, v232
	v_cvt_f32_i32_e32 v126, v126
	v_cvt_f32_i32_e32 v127, v127
	v_cvt_f32_i32_e32 v128, v128
	v_cvt_f32_i32_e32 v129, v129
	v_cvt_f32_i32_e32 v122, v122
	v_cvt_f32_i32_e32 v123, v123
	v_cvt_f32_i32_e32 v124, v124
	v_cvt_f32_i32_e32 v125, v125
	v_cvt_f32_i32_e32 v118, v118
	v_cvt_f32_i32_e32 v119, v119
	v_cvt_f32_i32_e32 v120, v120
	v_cvt_f32_i32_e32 v121, v121
	v_cvt_f32_i32_e32 v106, v106
	v_cvt_f32_i32_e32 v107, v107
	v_cvt_f32_i32_e32 v108, v108
	v_cvt_f32_i32_e32 v109, v109
	v_cvt_f32_i32_e32 v102, v102
	v_cvt_f32_i32_e32 v103, v103
	v_cvt_f32_i32_e32 v104, v104
	v_cvt_f32_i32_e32 v105, v105
	v_cvt_f32_i32_e32 v90, v90
	v_cvt_f32_i32_e32 v91, v91
	v_cvt_f32_i32_e32 v92, v92
	v_cvt_f32_i32_e32 v93, v93
	v_cvt_f32_i32_e32 v86, v86
	v_cvt_f32_i32_e32 v87, v87
	v_cvt_f32_i32_e32 v88, v88
	v_cvt_f32_i32_e32 v89, v89
	v_cvt_f32_i32_e32 v74, v74
	v_cvt_f32_i32_e32 v75, v75
	v_cvt_f32_i32_e32 v76, v76
	v_cvt_f32_i32_e32 v77, v77
	v_cvt_f32_i32_e32 v114, v114
	v_cvt_f32_i32_e32 v115, v115
	v_cvt_f32_i32_e32 v116, v116
	v_cvt_f32_i32_e32 v117, v117
	v_cvt_f32_i32_e32 v110, v110
	v_cvt_f32_i32_e32 v111, v111
	v_cvt_f32_i32_e32 v112, v112
	v_cvt_f32_i32_e32 v113, v113
	v_cvt_f32_i32_e32 v98, v98
	v_cvt_f32_i32_e32 v99, v99
	v_cvt_f32_i32_e32 v100, v100
	v_cvt_f32_i32_e32 v101, v101
	v_cvt_f32_i32_e32 v94, v94
	v_cvt_f32_i32_e32 v95, v95
	v_cvt_f32_i32_e32 v96, v96
	v_cvt_f32_i32_e32 v97, v97
	v_cvt_f32_i32_e32 v82, v82
	v_cvt_f32_i32_e32 v83, v83
	v_cvt_f32_i32_e32 v84, v84
	v_cvt_f32_i32_e32 v85, v85
	v_cvt_f32_i32_e32 v78, v78
	v_cvt_f32_i32_e32 v79, v79
	v_cvt_f32_i32_e32 v80, v80
	v_cvt_f32_i32_e32 v81, v81
	v_cvt_f32_i32_e32 v70, v70
	v_cvt_f32_i32_e32 v71, v71
	v_cvt_f32_i32_e32 v72, v72
	v_cvt_f32_i32_e32 v73, v73
	v_cvt_f32_i32_e32 v66, v66
	v_cvt_f32_i32_e32 v67, v67
	v_cvt_f32_i32_e32 v68, v68
	v_cvt_f32_i32_e32 v69, v69
	v_cvt_f32_i32_e32 v62, v62
	v_cvt_f32_i32_e32 v63, v63
	v_cvt_f32_i32_e32 v64, v64
	v_cvt_f32_i32_e32 v65, v65
	v_cvt_f32_i32_e32 v58, v58
	v_cvt_f32_i32_e32 v59, v59
	v_cvt_f32_i32_e32 v60, v60
	v_cvt_f32_i32_e32 v61, v61
	v_cvt_f32_i32_e32 v46, v46
	v_cvt_f32_i32_e32 v47, v47
	v_cvt_f32_i32_e32 v48, v48
	v_cvt_f32_i32_e32 v49, v49
	v_cvt_f32_i32_e32 v42, v42
	v_cvt_f32_i32_e32 v43, v43
	v_cvt_f32_i32_e32 v44, v44
	v_cvt_f32_i32_e32 v45, v45
	v_cvt_f32_i32_e32 v38, v38
	v_cvt_f32_i32_e32 v39, v39
	v_cvt_f32_i32_e32 v40, v40
	v_cvt_f32_i32_e32 v41, v41
	v_cvt_f32_i32_e32 v34, v34
	v_cvt_f32_i32_e32 v35, v35
	v_cvt_f32_i32_e32 v36, v36
	v_cvt_f32_i32_e32 v37, v37
	v_cvt_f32_i32_e32 v22, v22
	v_cvt_f32_i32_e32 v23, v23
	v_cvt_f32_i32_e32 v24, v24
	v_cvt_f32_i32_e32 v25, v25
	v_cvt_f32_i32_e32 v18, v18
	v_cvt_f32_i32_e32 v19, v19
	v_cvt_f32_i32_e32 v20, v20
	v_cvt_f32_i32_e32 v21, v21
	v_cvt_f32_i32_e32 v54, v54
	v_cvt_f32_i32_e32 v55, v55
	v_cvt_f32_i32_e32 v56, v56
	v_cvt_f32_i32_e32 v57, v57
	v_cvt_f32_i32_e32 v50, v50
	v_cvt_f32_i32_e32 v51, v51
	v_cvt_f32_i32_e32 v52, v52
	v_cvt_f32_i32_e32 v53, v53
	v_cvt_f32_i32_e32 v30, v30
	v_cvt_f32_i32_e32 v31, v31
	v_cvt_f32_i32_e32 v32, v32
	v_cvt_f32_i32_e32 v33, v33
	v_cvt_f32_i32_e32 v26, v26
	v_cvt_f32_i32_e32 v27, v27
	v_cvt_f32_i32_e32 v28, v28
	v_cvt_f32_i32_e32 v29, v29
	v_cvt_f32_i32_e32 v14, v14
	v_cvt_f32_i32_e32 v15, v15
	v_cvt_f32_i32_e32 v16, v16
	v_cvt_f32_i32_e32 v17, v17
	v_cvt_f32_i32_e32 v10, v10
	v_cvt_f32_i32_e32 v11, v11
	v_cvt_f32_i32_e32 v12, v12
	v_cvt_f32_i32_e32 v13, v13
	v_cvt_f32_i32_e32 v6, v6
	v_cvt_f32_i32_e32 v7, v7
	v_cvt_f32_i32_e32 v8, v8
	v_cvt_f32_i32_e32 v9, v9
	v_cvt_f32_i32_e32 v2, v2
	v_cvt_f32_i32_e32 v3, v3
	v_cvt_f32_i32_e32 v4, v4
	v_cvt_f32_i32_e32 v5, v5
	s_waitcnt lgkmcnt(0)
	v_mul_f32_e32 v194, 0x3a4d4011, v194
	v_mul_f32_e32 v196, 0x3a4d4011, v196
	v_mul_f32_e32 v198, 0x3a4d4011, v198
	v_mul_f32_e32 v200, 0x3a4d4011, v200
	v_mul_f32_e32 v202, 0x3a4d4011, v202
	v_mul_f32_e32 v204, 0x3a4d4011, v204
	v_mul_f32_e32 v206, 0x3a4d4011, v206
	v_mul_f32_e32 v208, 0x3a4d4011, v208
	v_pk_fma_f32 v[126:127], v[126:127], v[194:195], v[236:237] op_sel_hi:[1,0,1]
	v_pk_fma_f32 v[128:129], v[128:129], v[194:195], v[238:239] op_sel_hi:[1,0,1]
	v_pk_fma_f32 v[122:123], v[122:123], v[194:195], v[240:241] op_sel_hi:[1,0,1]
	v_pk_fma_f32 v[124:125], v[124:125], v[194:195], v[242:243] op_sel_hi:[1,0,1]
	v_pk_fma_f32 v[118:119], v[118:119], v[196:197], v[236:237] op_sel_hi:[1,0,1]
	v_pk_fma_f32 v[120:121], v[120:121], v[196:197], v[238:239] op_sel_hi:[1,0,1]
	v_pk_fma_f32 v[106:107], v[106:107], v[196:197], v[240:241] op_sel_hi:[1,0,1]
	v_pk_fma_f32 v[108:109], v[108:109], v[196:197], v[242:243] op_sel_hi:[1,0,1]
	v_pk_fma_f32 v[114:115], v[114:115], v[194:195], v[244:245] op_sel_hi:[1,0,1]
	v_pk_fma_f32 v[116:117], v[116:117], v[194:195], v[246:247] op_sel_hi:[1,0,1]
	v_pk_fma_f32 v[110:111], v[110:111], v[194:195], v[248:249] op_sel_hi:[1,0,1]
	v_pk_fma_f32 v[112:113], v[112:113], v[194:195], v[252:253] op_sel_hi:[1,0,1]
	v_pk_fma_f32 v[98:99], v[98:99], v[196:197], v[244:245] op_sel_hi:[1,0,1]
	v_pk_fma_f32 v[100:101], v[100:101], v[196:197], v[246:247] op_sel_hi:[1,0,1]
	v_pk_fma_f32 v[94:95], v[94:95], v[196:197], v[248:249] op_sel_hi:[1,0,1]
; __device__ __forceinline__ void swap16(int& x, int& y) { const auto r = __builtin_amdgcn_permlane16_swap((unsigned)x, (unsigned)y, false, false); x = (int)r[0]; y = (int)r[1]; }
;     __device__ __forceinline__ void operator()(const f32x4 (&acc)[2][2][4][2], const Unit& u, int wr, int wc, int fr, int fq) const {
;     ...
;                     const f32x4 gt = acc[ai][0][m][n] * descale + (n ? g1 : g0), up = acc[ai][1][m][n] * descale + (n ? u1 : u0);
; #pragma unroll
;                     for (int j = 0; j < 4; ++j) { const float g = fminf(gt[j], 7.0f), uu = fminf(fmaxf(up[j], -7.0f), 7.0f);
;                         const float sg = __builtin_amdgcn_rcpf(1.0f + __builtin_amdgcn_exp2f(g * (-1.702f * 1.4426950408889634f)));
;                         o[n][j] = (uu + 1.0f) * (g * sg) * oscale; }
;                 }
;                 w0[m] = __builtin_amdgcn_cvt_pk_fp8_f32(o[0][0], o[0][1], 0, false); w0[m] = __builtin_amdgcn_cvt_pk_fp8_f32(o[0][2], o[0][3], w0[m], true);
;                 w1[m] = __builtin_amdgcn_cvt_pk_fp8_f32(o[1][0], o[1][1], 0, false); w1[m] = __builtin_amdgcn_cvt_pk_fp8_f32(o[1][2], o[1][3], w1[m], true);
;             }
; #pragma unroll
;             for (int p = 0; p < 2; ++p) { swap16(w0[2 * p], w0[2 * p + 1]); swap16(w1[2 * p], w1[2 * p + 1]);
;                 u32x4 w; w.x = (unsigned)w0[2 * p]; w.y = (unsigned)w1[2 * p]; w.z = (unsigned)w0[2 * p + 1]; w.w = (unsigned)w1[2 * p + 1];
;                 *(u32x4*)(ACT + (size_t)(row0 + ai * HALF + (2 * p + odd) * 16) * DFF + colw) = w; }
	v_pk_fma_f32 v[96:97], v[96:97], v[196:197], v[252:253] op_sel_hi:[1,0,1]
	v_min_f32_e32 v126, 0x40e00000, v126
	v_min_f32_e32 v127, 0x40e00000, v127
	v_min_f32_e32 v128, 0x40e00000, v128
	v_min_f32_e32 v129, 0x40e00000, v129
	v_min_f32_e32 v122, 0x40e00000, v122
	v_min_f32_e32 v123, 0x40e00000, v123
	v_min_f32_e32 v124, 0x40e00000, v124
	v_min_f32_e32 v125, 0x40e00000, v125
	v_min_f32_e32 v118, 0x40e00000, v118
	v_min_f32_e32 v119, 0x40e00000, v119
	v_min_f32_e32 v120, 0x40e00000, v120
	v_min_f32_e32 v121, 0x40e00000, v121
	v_min_f32_e32 v106, 0x40e00000, v106
	v_min_f32_e32 v107, 0x40e00000, v107
	v_min_f32_e32 v108, 0x40e00000, v108
	v_min_f32_e32 v109, 0x40e00000, v109
	v_pk_mul_f32 v[210:211], v[126:127], s[98:99] op_sel_hi:[1,0]
	v_pk_mul_f32 v[212:213], v[128:129], s[98:99] op_sel_hi:[1,0]
	v_pk_mul_f32 v[214:215], v[122:123], s[98:99] op_sel_hi:[1,0]
	v_pk_mul_f32 v[216:217], v[124:125], s[98:99] op_sel_hi:[1,0]
	v_pk_mul_f32 v[218:219], v[118:119], s[98:99] op_sel_hi:[1,0]
	v_pk_mul_f32 v[220:221], v[120:121], s[98:99] op_sel_hi:[1,0]
	v_pk_mul_f32 v[222:223], v[106:107], s[98:99] op_sel_hi:[1,0]
	v_pk_mul_f32 v[224:225], v[108:109], s[98:99] op_sel_hi:[1,0]
	v_exp_f32_e32 v210, v210
	v_exp_f32_e32 v211, v211
	v_exp_f32_e32 v212, v212
	v_exp_f32_e32 v213, v213
	v_exp_f32_e32 v214, v214
	v_exp_f32_e32 v215, v215
	v_exp_f32_e32 v216, v216
	v_exp_f32_e32 v217, v217
	v_exp_f32_e32 v218, v218
	v_exp_f32_e32 v219, v219
	v_exp_f32_e32 v220, v220
	v_exp_f32_e32 v221, v221
	v_exp_f32_e32 v222, v222
	v_exp_f32_e32 v223, v223
	v_exp_f32_e32 v224, v224
	v_exp_f32_e32 v225, v225
	v_med3_f32 v114, v114, s65, v183
	v_med3_f32 v115, v115, s65, v183
	v_med3_f32 v116, v116, s65, v183
	v_med3_f32 v117, v117, s65, v183
	v_med3_f32 v110, v110, s65, v183
	v_med3_f32 v111, v111, s65, v183
	v_med3_f32 v112, v112, s65, v183
	v_med3_f32 v113, v113, s65, v183
	v_med3_f32 v98, v98, s65, v183
	v_med3_f32 v99, v99, s65, v183
	v_med3_f32 v100, v100, s65, v183
	v_med3_f32 v101, v101, s65, v183
	v_med3_f32 v94, v94, s65, v183
	v_med3_f32 v95, v95, s65, v183
	v_med3_f32 v96, v96, s65, v183
	v_med3_f32 v97, v97, s65, v183
	v_pk_add_f32 v[210:211], v[210:211], 1.0 op_sel_hi:[1,0]
	v_pk_add_f32 v[212:213], v[212:213], 1.0 op_sel_hi:[1,0]
	v_pk_add_f32 v[214:215], v[214:215], 1.0 op_sel_hi:[1,0]
	v_pk_add_f32 v[216:217], v[216:217], 1.0 op_sel_hi:[1,0]
	v_pk_add_f32 v[218:219], v[218:219], 1.0 op_sel_hi:[1,0]
	v_pk_add_f32 v[220:221], v[220:221], 1.0 op_sel_hi:[1,0]
	v_pk_add_f32 v[222:223], v[222:223], 1.0 op_sel_hi:[1,0]
	v_pk_add_f32 v[224:225], v[224:225], 1.0 op_sel_hi:[1,0]
	v_rcp_f32_e32 v210, v210
	v_rcp_f32_e32 v211, v211
	v_rcp_f32_e32 v212, v212
	v_rcp_f32_e32 v213, v213
	v_rcp_f32_e32 v214, v214
	v_rcp_f32_e32 v215, v215
	v_rcp_f32_e32 v216, v216
	v_rcp_f32_e32 v217, v217
	v_rcp_f32_e32 v218, v218
	v_rcp_f32_e32 v219, v219
	v_rcp_f32_e32 v220, v220
	v_rcp_f32_e32 v221, v221
	v_rcp_f32_e32 v222, v222
	v_rcp_f32_e32 v223, v223
	v_rcp_f32_e32 v224, v224
	v_rcp_f32_e32 v225, v225
	v_pk_fma_f32 v[114:115], v[114:115], 4.0, 4.0 op_sel_hi:[1,0,0]
	v_pk_fma_f32 v[116:117], v[116:117], 4.0, 4.0 op_sel_hi:[1,0,0]
	v_pk_fma_f32 v[110:111], v[110:111], 4.0, 4.0 op_sel_hi:[1,0,0]
	v_pk_fma_f32 v[112:113], v[112:113], 4.0, 4.0 op_sel_hi:[1,0,0]
	v_pk_fma_f32 v[98:99], v[98:99], 4.0, 4.0 op_sel_hi:[1,0,0]
	v_pk_fma_f32 v[100:101], v[100:101], 4.0, 4.0 op_sel_hi:[1,0,0]
	v_pk_fma_f32 v[94:95], v[94:95], 4.0, 4.0 op_sel_hi:[1,0,0]
	v_pk_fma_f32 v[96:97], v[96:97], 4.0, 4.0 op_sel_hi:[1,0,0]
	v_pk_mul_f32 v[126:127], v[126:127], v[210:211]
	v_pk_mul_f32 v[128:129], v[128:129], v[212:213]
	v_pk_mul_f32 v[122:123], v[122:123], v[214:215]
	v_pk_mul_f32 v[124:125], v[124:125], v[216:217]
	v_pk_mul_f32 v[118:119], v[118:119], v[218:219]
	v_pk_mul_f32 v[120:121], v[120:121], v[220:221]
	v_pk_mul_f32 v[106:107], v[106:107], v[222:223]
	v_pk_mul_f32 v[108:109], v[108:109], v[224:225]
	v_pk_mul_f32 v[126:127], v[126:127], v[114:115]
	v_pk_mul_f32 v[128:129], v[128:129], v[116:117]
	v_pk_mul_f32 v[122:123], v[122:123], v[110:111]
	v_pk_mul_f32 v[124:125], v[124:125], v[112:113]
	v_pk_mul_f32 v[118:119], v[118:119], v[98:99]
	v_pk_mul_f32 v[120:121], v[120:121], v[100:101]
	v_pk_mul_f32 v[106:107], v[106:107], v[94:95]
	v_pk_mul_f32 v[108:109], v[108:109], v[96:97]
	v_cvt_pk_fp8_f32 v226, v126, v127
	v_cvt_pk_fp8_f32 v226, v128, v129 op_sel:[0,0,1]
	v_cvt_pk_fp8_f32 v227, v122, v123
	v_cvt_pk_fp8_f32 v227, v124, v125 op_sel:[0,0,1]
	v_cvt_pk_fp8_f32 v228, v118, v119
	v_cvt_pk_fp8_f32 v228, v120, v121 op_sel:[0,0,1]
	v_cvt_pk_fp8_f32 v229, v106, v107
	v_cvt_pk_fp8_f32 v229, v108, v109 op_sel:[0,0,1]
	v_or_b32_e32 v230, v232, v172
	v_ashrrev_i32_e32 v231, 31, v230
	v_lshlrev_b64 v[230:231], 11, v[230:231]
	v_permlane16_swap_b32_e32 v226, v228
	v_permlane16_swap_b32_e32 v227, v229
	v_lshl_add_u64 v[230:231], s[16:17], 0, v[230:231]
	v_lshl_add_u64 v[230:231], v[230:231], 0, v[130:131]
	global_store_dwordx4 v[230:231], v[226:229], off
	v_pk_fma_f32 v[102:103], v[102:103], v[198:199], v[236:237] op_sel_hi:[1,0,1]
	v_pk_fma_f32 v[104:105], v[104:105], v[198:199], v[238:239] op_sel_hi:[1,0,1]
	v_pk_fma_f32 v[90:91], v[90:91], v[198:199], v[240:241] op_sel_hi:[1,0,1]
	v_pk_fma_f32 v[92:93], v[92:93], v[198:199], v[242:243] op_sel_hi:[1,0,1]
	v_pk_fma_f32 v[86:87], v[86:87], v[200:201], v[236:237] op_sel_hi:[1,0,1]
	v_pk_fma_f32 v[88:89], v[88:89], v[200:201], v[238:239] op_sel_hi:[1,0,1]
	v_pk_fma_f32 v[74:75], v[74:75], v[200:201], v[240:241] op_sel_hi:[1,0,1]
	v_pk_fma_f32 v[76:77], v[76:77], v[200:201], v[242:243] op_sel_hi:[1,0,1]
	v_pk_fma_f32 v[82:83], v[82:83], v[198:199], v[244:245] op_sel_hi:[1,0,1]
; __device__ __forceinline__ void swap16(int& x, int& y) { const auto r = __builtin_amdgcn_permlane16_swap((unsigned)x, (unsigned)y, false, false); x = (int)r[0]; y = (int)r[1]; }
;     __device__ __forceinline__ void operator()(const f32x4 (&acc)[2][2][4][2], const Unit& u, int wr, int wc, int fr, int fq) const {
;     ...
;                     const f32x4 gt = acc[ai][0][m][n] * descale + (n ? g1 : g0), up = acc[ai][1][m][n] * descale + (n ? u1 : u0);
; #pragma unroll
;                     for (int j = 0; j < 4; ++j) { const float g = fminf(gt[j], 7.0f), uu = fminf(fmaxf(up[j], -7.0f), 7.0f);
;                         const float sg = __builtin_amdgcn_rcpf(1.0f + __builtin_amdgcn_exp2f(g * (-1.702f * 1.4426950408889634f)));
;                         o[n][j] = (uu + 1.0f) * (g * sg) * oscale; }
;                 }
;                 w0[m] = __builtin_amdgcn_cvt_pk_fp8_f32(o[0][0], o[0][1], 0, false); w0[m] = __builtin_amdgcn_cvt_pk_fp8_f32(o[0][2], o[0][3], w0[m], true);
;                 w1[m] = __builtin_amdgcn_cvt_pk_fp8_f32(o[1][0], o[1][1], 0, false); w1[m] = __builtin_amdgcn_cvt_pk_fp8_f32(o[1][2], o[1][3], w1[m], true);
;             }
; #pragma unroll
;             for (int p = 0; p < 2; ++p) { swap16(w0[2 * p], w0[2 * p + 1]); swap16(w1[2 * p], w1[2 * p + 1]);
;                 u32x4 w; w.x = (unsigned)w0[2 * p]; w.y = (unsigned)w1[2 * p]; w.z = (unsigned)w0[2 * p + 1]; w.w = (unsigned)w1[2 * p + 1];
;                 *(u32x4*)(ACT + (size_t)(row0 + ai * HALF + (2 * p + odd) * 16) * DFF + colw) = w; }
	v_pk_fma_f32 v[84:85], v[84:85], v[198:199], v[246:247] op_sel_hi:[1,0,1]
	v_pk_fma_f32 v[78:79], v[78:79], v[198:199], v[248:249] op_sel_hi:[1,0,1]
	v_pk_fma_f32 v[80:81], v[80:81], v[198:199], v[252:253] op_sel_hi:[1,0,1]
	v_pk_fma_f32 v[70:71], v[70:71], v[200:201], v[244:245] op_sel_hi:[1,0,1]
	v_pk_fma_f32 v[72:73], v[72:73], v[200:201], v[246:247] op_sel_hi:[1,0,1]
	v_pk_fma_f32 v[66:67], v[66:67], v[200:201], v[248:249] op_sel_hi:[1,0,1]
	v_pk_fma_f32 v[68:69], v[68:69], v[200:201], v[252:253] op_sel_hi:[1,0,1]
	v_min_f32_e32 v102, 0x40e00000, v102
	v_min_f32_e32 v103, 0x40e00000, v103
	v_min_f32_e32 v104, 0x40e00000, v104
	v_min_f32_e32 v105, 0x40e00000, v105
	v_min_f32_e32 v90, 0x40e00000, v90
	v_min_f32_e32 v91, 0x40e00000, v91
	v_min_f32_e32 v92, 0x40e00000, v92
	v_min_f32_e32 v93, 0x40e00000, v93
	v_min_f32_e32 v86, 0x40e00000, v86
	v_min_f32_e32 v87, 0x40e00000, v87
	v_min_f32_e32 v88, 0x40e00000, v88
	v_min_f32_e32 v89, 0x40e00000, v89
	v_min_f32_e32 v74, 0x40e00000, v74
	v_min_f32_e32 v75, 0x40e00000, v75
	v_min_f32_e32 v76, 0x40e00000, v76
	v_min_f32_e32 v77, 0x40e00000, v77
	v_pk_mul_f32 v[210:211], v[102:103], s[98:99] op_sel_hi:[1,0]
	v_pk_mul_f32 v[212:213], v[104:105], s[98:99] op_sel_hi:[1,0]
	v_pk_mul_f32 v[214:215], v[90:91], s[98:99] op_sel_hi:[1,0]
	v_pk_mul_f32 v[216:217], v[92:93], s[98:99] op_sel_hi:[1,0]
	v_pk_mul_f32 v[218:219], v[86:87], s[98:99] op_sel_hi:[1,0]
	v_pk_mul_f32 v[220:221], v[88:89], s[98:99] op_sel_hi:[1,0]
	v_pk_mul_f32 v[222:223], v[74:75], s[98:99] op_sel_hi:[1,0]
	v_pk_mul_f32 v[224:225], v[76:77], s[98:99] op_sel_hi:[1,0]
	v_exp_f32_e32 v210, v210
	v_exp_f32_e32 v211, v211
	v_exp_f32_e32 v212, v212
	v_exp_f32_e32 v213, v213
	v_exp_f32_e32 v214, v214
	v_exp_f32_e32 v215, v215
	v_exp_f32_e32 v216, v216
	v_exp_f32_e32 v217, v217
	v_exp_f32_e32 v218, v218
	v_exp_f32_e32 v219, v219
	v_exp_f32_e32 v220, v220
	v_exp_f32_e32 v221, v221
	v_exp_f32_e32 v222, v222
	v_exp_f32_e32 v223, v223
	v_exp_f32_e32 v224, v224
	v_exp_f32_e32 v225, v225
	v_med3_f32 v82, v82, s65, v183
	v_med3_f32 v83, v83, s65, v183
	v_med3_f32 v84, v84, s65, v183
	v_med3_f32 v85, v85, s65, v183
	v_med3_f32 v78, v78, s65, v183
	v_med3_f32 v79, v79, s65, v183
	v_med3_f32 v80, v80, s65, v183
	v_med3_f32 v81, v81, s65, v183
	v_med3_f32 v70, v70, s65, v183
	v_med3_f32 v71, v71, s65, v183
	v_med3_f32 v72, v72, s65, v183
	v_med3_f32 v73, v73, s65, v183
	v_med3_f32 v66, v66, s65, v183
	v_med3_f32 v67, v67, s65, v183
	v_med3_f32 v68, v68, s65, v183
	v_med3_f32 v69, v69, s65, v183
	v_pk_add_f32 v[210:211], v[210:211], 1.0 op_sel_hi:[1,0]
	v_pk_add_f32 v[212:213], v[212:213], 1.0 op_sel_hi:[1,0]
	v_pk_add_f32 v[214:215], v[214:215], 1.0 op_sel_hi:[1,0]
	v_pk_add_f32 v[216:217], v[216:217], 1.0 op_sel_hi:[1,0]
	v_pk_add_f32 v[218:219], v[218:219], 1.0 op_sel_hi:[1,0]
	v_pk_add_f32 v[220:221], v[220:221], 1.0 op_sel_hi:[1,0]
	v_pk_add_f32 v[222:223], v[222:223], 1.0 op_sel_hi:[1,0]
	v_pk_add_f32 v[224:225], v[224:225], 1.0 op_sel_hi:[1,0]
	v_rcp_f32_e32 v210, v210
	v_rcp_f32_e32 v211, v211
	v_rcp_f32_e32 v212, v212
	v_rcp_f32_e32 v213, v213
	v_rcp_f32_e32 v214, v214
	v_rcp_f32_e32 v215, v215
	v_rcp_f32_e32 v216, v216
	v_rcp_f32_e32 v217, v217
	v_rcp_f32_e32 v218, v218
	v_rcp_f32_e32 v219, v219
	v_rcp_f32_e32 v220, v220
	v_rcp_f32_e32 v221, v221
	v_rcp_f32_e32 v222, v222
	v_rcp_f32_e32 v223, v223
	v_rcp_f32_e32 v224, v224
	v_rcp_f32_e32 v225, v225
	v_pk_fma_f32 v[82:83], v[82:83], 4.0, 4.0 op_sel_hi:[1,0,0]
	v_pk_fma_f32 v[84:85], v[84:85], 4.0, 4.0 op_sel_hi:[1,0,0]
	v_pk_fma_f32 v[78:79], v[78:79], 4.0, 4.0 op_sel_hi:[1,0,0]
	v_pk_fma_f32 v[80:81], v[80:81], 4.0, 4.0 op_sel_hi:[1,0,0]
	v_pk_fma_f32 v[70:71], v[70:71], 4.0, 4.0 op_sel_hi:[1,0,0]
	v_pk_fma_f32 v[72:73], v[72:73], 4.0, 4.0 op_sel_hi:[1,0,0]
	v_pk_fma_f32 v[66:67], v[66:67], 4.0, 4.0 op_sel_hi:[1,0,0]
	v_pk_fma_f32 v[68:69], v[68:69], 4.0, 4.0 op_sel_hi:[1,0,0]
	v_pk_mul_f32 v[102:103], v[102:103], v[210:211]
	v_pk_mul_f32 v[104:105], v[104:105], v[212:213]
	v_pk_mul_f32 v[90:91], v[90:91], v[214:215]
	v_pk_mul_f32 v[92:93], v[92:93], v[216:217]
	v_pk_mul_f32 v[86:87], v[86:87], v[218:219]
	v_pk_mul_f32 v[88:89], v[88:89], v[220:221]
	v_pk_mul_f32 v[74:75], v[74:75], v[222:223]
	v_pk_mul_f32 v[76:77], v[76:77], v[224:225]
	v_pk_mul_f32 v[102:103], v[102:103], v[82:83]
	v_pk_mul_f32 v[104:105], v[104:105], v[84:85]
	v_pk_mul_f32 v[90:91], v[90:91], v[78:79]
	v_pk_mul_f32 v[92:93], v[92:93], v[80:81]
	v_pk_mul_f32 v[86:87], v[86:87], v[70:71]
	v_pk_mul_f32 v[88:89], v[88:89], v[72:73]
	v_pk_mul_f32 v[74:75], v[74:75], v[66:67]
	v_pk_mul_f32 v[76:77], v[76:77], v[68:69]
	v_cvt_pk_fp8_f32 v132, v102, v103
	v_cvt_pk_fp8_f32 v132, v104, v105 op_sel:[0,0,1]
	v_cvt_pk_fp8_f32 v133, v90, v91
	v_cvt_pk_fp8_f32 v133, v92, v93 op_sel:[0,0,1]
	v_cvt_pk_fp8_f32 v134, v86, v87
	v_cvt_pk_fp8_f32 v134, v88, v89 op_sel:[0,0,1]
	v_cvt_pk_fp8_f32 v135, v74, v75
	v_cvt_pk_fp8_f32 v135, v76, v77 op_sel:[0,0,1]
	v_or_b32_e32 v230, v232, v173
	v_ashrrev_i32_e32 v231, 31, v230
	v_lshlrev_b64 v[230:231], 11, v[230:231]
	v_permlane16_swap_b32_e32 v132, v134
	v_permlane16_swap_b32_e32 v133, v135
	v_lshl_add_u64 v[230:231], s[16:17], 0, v[230:231]
	v_lshl_add_u64 v[230:231], v[230:231], 0, v[130:131]
	global_store_dwordx4 v[230:231], v[132:135], off
	v_pk_fma_f32 v[62:63], v[62:63], v[202:203], v[236:237] op_sel_hi:[1,0,1]
	v_pk_fma_f32 v[64:65], v[64:65], v[202:203], v[238:239] op_sel_hi:[1,0,1]
	v_pk_fma_f32 v[58:59], v[58:59], v[202:203], v[240:241] op_sel_hi:[1,0,1]
	v_pk_fma_f32 v[60:61], v[60:61], v[202:203], v[242:243] op_sel_hi:[1,0,1]
	v_pk_fma_f32 v[46:47], v[46:47], v[204:205], v[236:237] op_sel_hi:[1,0,1]
; __device__ __forceinline__ void swap16(int& x, int& y) { const auto r = __builtin_amdgcn_permlane16_swap((unsigned)x, (unsigned)y, false, false); x = (int)r[0]; y = (int)r[1]; }
;     __device__ __forceinline__ void operator()(const f32x4 (&acc)[2][2][4][2], const Unit& u, int wr, int wc, int fr, int fq) const {
;     ...
;                     const f32x4 gt = acc[ai][0][m][n] * descale + (n ? g1 : g0), up = acc[ai][1][m][n] * descale + (n ? u1 : u0);
; #pragma unroll
;                     for (int j = 0; j < 4; ++j) { const float g = fminf(gt[j], 7.0f), uu = fminf(fmaxf(up[j], -7.0f), 7.0f);
;                         const float sg = __builtin_amdgcn_rcpf(1.0f + __builtin_amdgcn_exp2f(g * (-1.702f * 1.4426950408889634f)));
;                         o[n][j] = (uu + 1.0f) * (g * sg) * oscale; }
;                 }
;                 w0[m] = __builtin_amdgcn_cvt_pk_fp8_f32(o[0][0], o[0][1], 0, false); w0[m] = __builtin_amdgcn_cvt_pk_fp8_f32(o[0][2], o[0][3], w0[m], true);
;                 w1[m] = __builtin_amdgcn_cvt_pk_fp8_f32(o[1][0], o[1][1], 0, false); w1[m] = __builtin_amdgcn_cvt_pk_fp8_f32(o[1][2], o[1][3], w1[m], true);
;             }
; #pragma unroll
;             for (int p = 0; p < 2; ++p) { swap16(w0[2 * p], w0[2 * p + 1]); swap16(w1[2 * p], w1[2 * p + 1]);
;                 u32x4 w; w.x = (unsigned)w0[2 * p]; w.y = (unsigned)w1[2 * p]; w.z = (unsigned)w0[2 * p + 1]; w.w = (unsigned)w1[2 * p + 1];
;                 *(u32x4*)(ACT + (size_t)(row0 + ai * HALF + (2 * p + odd) * 16) * DFF + colw) = w; }
	v_pk_fma_f32 v[48:49], v[48:49], v[204:205], v[238:239] op_sel_hi:[1,0,1]
	v_pk_fma_f32 v[42:43], v[42:43], v[204:205], v[240:241] op_sel_hi:[1,0,1]
	v_pk_fma_f32 v[44:45], v[44:45], v[204:205], v[242:243] op_sel_hi:[1,0,1]
	v_pk_fma_f32 v[54:55], v[54:55], v[202:203], v[244:245] op_sel_hi:[1,0,1]
	v_pk_fma_f32 v[56:57], v[56:57], v[202:203], v[246:247] op_sel_hi:[1,0,1]
	v_pk_fma_f32 v[50:51], v[50:51], v[202:203], v[248:249] op_sel_hi:[1,0,1]
	v_pk_fma_f32 v[52:53], v[52:53], v[202:203], v[252:253] op_sel_hi:[1,0,1]
	v_pk_fma_f32 v[30:31], v[30:31], v[204:205], v[244:245] op_sel_hi:[1,0,1]
	v_pk_fma_f32 v[32:33], v[32:33], v[204:205], v[246:247] op_sel_hi:[1,0,1]
	v_pk_fma_f32 v[26:27], v[26:27], v[204:205], v[248:249] op_sel_hi:[1,0,1]
	v_pk_fma_f32 v[28:29], v[28:29], v[204:205], v[252:253] op_sel_hi:[1,0,1]
	v_min_f32_e32 v62, 0x40e00000, v62
	v_min_f32_e32 v63, 0x40e00000, v63
	v_min_f32_e32 v64, 0x40e00000, v64
	v_min_f32_e32 v65, 0x40e00000, v65
	v_min_f32_e32 v58, 0x40e00000, v58
	v_min_f32_e32 v59, 0x40e00000, v59
	v_min_f32_e32 v60, 0x40e00000, v60
	v_min_f32_e32 v61, 0x40e00000, v61
	v_min_f32_e32 v46, 0x40e00000, v46
	v_min_f32_e32 v47, 0x40e00000, v47
	v_min_f32_e32 v48, 0x40e00000, v48
	v_min_f32_e32 v49, 0x40e00000, v49
	v_min_f32_e32 v42, 0x40e00000, v42
	v_min_f32_e32 v43, 0x40e00000, v43
	v_min_f32_e32 v44, 0x40e00000, v44
	v_min_f32_e32 v45, 0x40e00000, v45
	v_pk_mul_f32 v[210:211], v[62:63], s[98:99] op_sel_hi:[1,0]
	v_pk_mul_f32 v[212:213], v[64:65], s[98:99] op_sel_hi:[1,0]
	v_pk_mul_f32 v[214:215], v[58:59], s[98:99] op_sel_hi:[1,0]
	v_pk_mul_f32 v[216:217], v[60:61], s[98:99] op_sel_hi:[1,0]
	v_pk_mul_f32 v[218:219], v[46:47], s[98:99] op_sel_hi:[1,0]
	v_pk_mul_f32 v[220:221], v[48:49], s[98:99] op_sel_hi:[1,0]
	v_pk_mul_f32 v[222:223], v[42:43], s[98:99] op_sel_hi:[1,0]
	v_pk_mul_f32 v[224:225], v[44:45], s[98:99] op_sel_hi:[1,0]
	v_exp_f32_e32 v210, v210
	v_exp_f32_e32 v211, v211
	v_exp_f32_e32 v212, v212
	v_exp_f32_e32 v213, v213
	v_exp_f32_e32 v214, v214
	v_exp_f32_e32 v215, v215
	v_exp_f32_e32 v216, v216
	v_exp_f32_e32 v217, v217
	v_exp_f32_e32 v218, v218
	v_exp_f32_e32 v219, v219
	v_exp_f32_e32 v220, v220
	v_exp_f32_e32 v221, v221
	v_exp_f32_e32 v222, v222
	v_exp_f32_e32 v223, v223
	v_exp_f32_e32 v224, v224
	v_exp_f32_e32 v225, v225
	v_med3_f32 v54, v54, s65, v183
	v_med3_f32 v55, v55, s65, v183
	v_med3_f32 v56, v56, s65, v183
	v_med3_f32 v57, v57, s65, v183
	v_med3_f32 v50, v50, s65, v183
	v_med3_f32 v51, v51, s65, v183
	v_med3_f32 v52, v52, s65, v183
	v_med3_f32 v53, v53, s65, v183
	v_med3_f32 v30, v30, s65, v183
	v_med3_f32 v31, v31, s65, v183
	v_med3_f32 v32, v32, s65, v183
	v_med3_f32 v33, v33, s65, v183
	v_med3_f32 v26, v26, s65, v183
	v_med3_f32 v27, v27, s65, v183
	v_med3_f32 v28, v28, s65, v183
	v_med3_f32 v29, v29, s65, v183
	v_pk_add_f32 v[210:211], v[210:211], 1.0 op_sel_hi:[1,0]
	v_pk_add_f32 v[212:213], v[212:213], 1.0 op_sel_hi:[1,0]
	v_pk_add_f32 v[214:215], v[214:215], 1.0 op_sel_hi:[1,0]
	v_pk_add_f32 v[216:217], v[216:217], 1.0 op_sel_hi:[1,0]
	v_pk_add_f32 v[218:219], v[218:219], 1.0 op_sel_hi:[1,0]
	v_pk_add_f32 v[220:221], v[220:221], 1.0 op_sel_hi:[1,0]
	v_pk_add_f32 v[222:223], v[222:223], 1.0 op_sel_hi:[1,0]
	v_pk_add_f32 v[224:225], v[224:225], 1.0 op_sel_hi:[1,0]
	v_rcp_f32_e32 v210, v210
	v_rcp_f32_e32 v211, v211
	v_rcp_f32_e32 v212, v212
	v_rcp_f32_e32 v213, v213
	v_rcp_f32_e32 v214, v214
	v_rcp_f32_e32 v215, v215
	v_rcp_f32_e32 v216, v216
	v_rcp_f32_e32 v217, v217
	v_rcp_f32_e32 v218, v218
	v_rcp_f32_e32 v219, v219
	v_rcp_f32_e32 v220, v220
	v_rcp_f32_e32 v221, v221
	v_rcp_f32_e32 v222, v222
	v_rcp_f32_e32 v223, v223
	v_rcp_f32_e32 v224, v224
	v_rcp_f32_e32 v225, v225
	v_pk_fma_f32 v[54:55], v[54:55], 4.0, 4.0 op_sel_hi:[1,0,0]
	v_pk_fma_f32 v[56:57], v[56:57], 4.0, 4.0 op_sel_hi:[1,0,0]
	v_pk_fma_f32 v[50:51], v[50:51], 4.0, 4.0 op_sel_hi:[1,0,0]
	v_pk_fma_f32 v[52:53], v[52:53], 4.0, 4.0 op_sel_hi:[1,0,0]
	v_pk_fma_f32 v[30:31], v[30:31], 4.0, 4.0 op_sel_hi:[1,0,0]
	v_pk_fma_f32 v[32:33], v[32:33], 4.0, 4.0 op_sel_hi:[1,0,0]
	v_pk_fma_f32 v[26:27], v[26:27], 4.0, 4.0 op_sel_hi:[1,0,0]
	v_pk_fma_f32 v[28:29], v[28:29], 4.0, 4.0 op_sel_hi:[1,0,0]
	v_pk_mul_f32 v[62:63], v[62:63], v[210:211]
	v_pk_mul_f32 v[64:65], v[64:65], v[212:213]
	v_pk_mul_f32 v[58:59], v[58:59], v[214:215]
	v_pk_mul_f32 v[60:61], v[60:61], v[216:217]
	v_pk_mul_f32 v[46:47], v[46:47], v[218:219]
	v_pk_mul_f32 v[48:49], v[48:49], v[220:221]
	v_pk_mul_f32 v[42:43], v[42:43], v[222:223]
	v_pk_mul_f32 v[44:45], v[44:45], v[224:225]
	v_pk_mul_f32 v[62:63], v[62:63], v[54:55]
	v_pk_mul_f32 v[64:65], v[64:65], v[56:57]
	v_pk_mul_f32 v[58:59], v[58:59], v[50:51]
	v_pk_mul_f32 v[60:61], v[60:61], v[52:53]
	v_pk_mul_f32 v[46:47], v[46:47], v[30:31]
	v_pk_mul_f32 v[48:49], v[48:49], v[32:33]
	v_pk_mul_f32 v[42:43], v[42:43], v[26:27]
	v_pk_mul_f32 v[44:45], v[44:45], v[28:29]
	v_cvt_pk_fp8_f32 v136, v62, v63
	v_cvt_pk_fp8_f32 v136, v64, v65 op_sel:[0,0,1]
	v_cvt_pk_fp8_f32 v137, v58, v59
	v_cvt_pk_fp8_f32 v137, v60, v61 op_sel:[0,0,1]
	v_cvt_pk_fp8_f32 v138, v46, v47
	v_cvt_pk_fp8_f32 v138, v48, v49 op_sel:[0,0,1]
	v_cvt_pk_fp8_f32 v139, v42, v43
	v_cvt_pk_fp8_f32 v139, v44, v45 op_sel:[0,0,1]
	v_or_b32_e32 v230, v233, v172
	v_ashrrev_i32_e32 v231, 31, v230
	v_lshlrev_b64 v[230:231], 11, v[230:231]
	v_permlane16_swap_b32_e32 v136, v138
	v_permlane16_swap_b32_e32 v137, v139
	v_lshl_add_u64 v[230:231], s[16:17], 0, v[230:231]
	v_lshl_add_u64 v[230:231], v[230:231], 0, v[130:131]
	global_store_dwordx4 v[230:231], v[136:139], off
	v_pk_fma_f32 v[38:39], v[38:39], v[206:207], v[236:237] op_sel_hi:[1,0,1]
; __device__ __forceinline__ void swap16(int& x, int& y) { const auto r = __builtin_amdgcn_permlane16_swap((unsigned)x, (unsigned)y, false, false); x = (int)r[0]; y = (int)r[1]; }
; #define PG8_BAR __builtin_amdgcn_s_barrier()
;     __device__ __forceinline__ void operator()(const f32x4 (&acc)[2][2][4][2], const Unit& u, int wr, int wc, int fr, int fq) const {
;     ...
;                     const f32x4 gt = acc[ai][0][m][n] * descale + (n ? g1 : g0), up = acc[ai][1][m][n] * descale + (n ? u1 : u0);
; #pragma unroll
;                     for (int j = 0; j < 4; ++j) { const float g = fminf(gt[j], 7.0f), uu = fminf(fmaxf(up[j], -7.0f), 7.0f);
;                         const float sg = __builtin_amdgcn_rcpf(1.0f + __builtin_amdgcn_exp2f(g * (-1.702f * 1.4426950408889634f)));
;                         o[n][j] = (uu + 1.0f) * (g * sg) * oscale; }
;                 }
;                 w0[m] = __builtin_amdgcn_cvt_pk_fp8_f32(o[0][0], o[0][1], 0, false); w0[m] = __builtin_amdgcn_cvt_pk_fp8_f32(o[0][2], o[0][3], w0[m], true);
;                 w1[m] = __builtin_amdgcn_cvt_pk_fp8_f32(o[1][0], o[1][1], 0, false); w1[m] = __builtin_amdgcn_cvt_pk_fp8_f32(o[1][2], o[1][3], w1[m], true);
;             }
; #pragma unroll
;             for (int p = 0; p < 2; ++p) { swap16(w0[2 * p], w0[2 * p + 1]); swap16(w1[2 * p], w1[2 * p + 1]);
;                 u32x4 w; w.x = (unsigned)w0[2 * p]; w.y = (unsigned)w1[2 * p]; w.z = (unsigned)w0[2 * p + 1]; w.w = (unsigned)w1[2 * p + 1];
;                 *(u32x4*)(ACT + (size_t)(row0 + ai * HALF + (2 * p + odd) * 16) * DFF + colw) = w; }
; template <class Epi, bool GATHER, int MODE, bool SPLIT = false>
; __device__ __forceinline__ void gemm_phase(PG8_LAS unsigned char* lds, const Gemm g, const Order& S, const Epi& E) {
;     ...
;         if (!has_next) break;
; #pragma unroll
;         for (int a = 0; a < 2; ++a)
; #pragma unroll
;             for (int b = 0; b < 2; ++b)
; #pragma unroll
;                 for (int m = 0; m < 4; ++m)
; #pragma unroll
;                     for (int n = 0; n < 2; ++n) acc[a][b][m][n] = (f32x4){0.f, 0.f, 0.f, 0.f};
;         cur = nxt; cB = nB; cAr = nAr; ++ui;
; #pragma unroll
;         for (int h = 0; h < 2; ++h)
; #pragma unroll
;             for (int i = 0; i < 2; ++i) cv[h][i] = nv[h][i];
;         if (wr == 1) PG8_BAR;
	v_pk_fma_f32 v[40:41], v[40:41], v[206:207], v[238:239] op_sel_hi:[1,0,1]
	v_pk_fma_f32 v[34:35], v[34:35], v[206:207], v[240:241] op_sel_hi:[1,0,1]
	v_pk_fma_f32 v[36:37], v[36:37], v[206:207], v[242:243] op_sel_hi:[1,0,1]
	v_pk_fma_f32 v[22:23], v[22:23], v[208:209], v[236:237] op_sel_hi:[1,0,1]
	v_pk_fma_f32 v[24:25], v[24:25], v[208:209], v[238:239] op_sel_hi:[1,0,1]
	v_pk_fma_f32 v[18:19], v[18:19], v[208:209], v[240:241] op_sel_hi:[1,0,1]
	v_pk_fma_f32 v[20:21], v[20:21], v[208:209], v[242:243] op_sel_hi:[1,0,1]
	v_pk_fma_f32 v[14:15], v[14:15], v[206:207], v[244:245] op_sel_hi:[1,0,1]
	v_pk_fma_f32 v[16:17], v[16:17], v[206:207], v[246:247] op_sel_hi:[1,0,1]
	v_pk_fma_f32 v[10:11], v[10:11], v[206:207], v[248:249] op_sel_hi:[1,0,1]
	v_pk_fma_f32 v[12:13], v[12:13], v[206:207], v[252:253] op_sel_hi:[1,0,1]
	v_pk_fma_f32 v[6:7], v[6:7], v[208:209], v[244:245] op_sel_hi:[1,0,1]
	v_pk_fma_f32 v[8:9], v[8:9], v[208:209], v[246:247] op_sel_hi:[1,0,1]
	v_pk_fma_f32 v[2:3], v[2:3], v[208:209], v[248:249] op_sel_hi:[1,0,1]
	v_pk_fma_f32 v[4:5], v[4:5], v[208:209], v[252:253] op_sel_hi:[1,0,1]
	v_min_f32_e32 v38, 0x40e00000, v38
	v_min_f32_e32 v39, 0x40e00000, v39
	v_min_f32_e32 v40, 0x40e00000, v40
	v_min_f32_e32 v41, 0x40e00000, v41
	v_min_f32_e32 v34, 0x40e00000, v34
	v_min_f32_e32 v35, 0x40e00000, v35
	v_min_f32_e32 v36, 0x40e00000, v36
	v_min_f32_e32 v37, 0x40e00000, v37
	v_min_f32_e32 v22, 0x40e00000, v22
	v_min_f32_e32 v23, 0x40e00000, v23
	v_min_f32_e32 v24, 0x40e00000, v24
	v_min_f32_e32 v25, 0x40e00000, v25
	v_min_f32_e32 v18, 0x40e00000, v18
	v_min_f32_e32 v19, 0x40e00000, v19
	v_min_f32_e32 v20, 0x40e00000, v20
	v_min_f32_e32 v21, 0x40e00000, v21
	v_pk_mul_f32 v[210:211], v[38:39], s[98:99] op_sel_hi:[1,0]
	v_pk_mul_f32 v[212:213], v[40:41], s[98:99] op_sel_hi:[1,0]
	v_pk_mul_f32 v[214:215], v[34:35], s[98:99] op_sel_hi:[1,0]
	v_pk_mul_f32 v[216:217], v[36:37], s[98:99] op_sel_hi:[1,0]
	v_pk_mul_f32 v[218:219], v[22:23], s[98:99] op_sel_hi:[1,0]
	v_pk_mul_f32 v[220:221], v[24:25], s[98:99] op_sel_hi:[1,0]
	v_pk_mul_f32 v[222:223], v[18:19], s[98:99] op_sel_hi:[1,0]
	v_pk_mul_f32 v[224:225], v[20:21], s[98:99] op_sel_hi:[1,0]
	v_exp_f32_e32 v210, v210
	v_exp_f32_e32 v211, v211
	v_exp_f32_e32 v212, v212
	v_exp_f32_e32 v213, v213
	v_exp_f32_e32 v214, v214
	v_exp_f32_e32 v215, v215
	v_exp_f32_e32 v216, v216
	v_exp_f32_e32 v217, v217
	v_exp_f32_e32 v218, v218
	v_exp_f32_e32 v219, v219
	v_exp_f32_e32 v220, v220
	v_exp_f32_e32 v221, v221
	v_exp_f32_e32 v222, v222
	v_exp_f32_e32 v223, v223
	v_exp_f32_e32 v224, v224
	v_exp_f32_e32 v225, v225
	v_med3_f32 v14, v14, s65, v183
	v_med3_f32 v15, v15, s65, v183
	v_med3_f32 v16, v16, s65, v183
	v_med3_f32 v17, v17, s65, v183
	v_med3_f32 v10, v10, s65, v183
	v_med3_f32 v11, v11, s65, v183
	v_med3_f32 v12, v12, s65, v183
	v_med3_f32 v13, v13, s65, v183
	v_med3_f32 v6, v6, s65, v183
	v_med3_f32 v7, v7, s65, v183
	v_med3_f32 v8, v8, s65, v183
	v_med3_f32 v9, v9, s65, v183
	v_med3_f32 v2, v2, s65, v183
	v_med3_f32 v3, v3, s65, v183
	v_med3_f32 v4, v4, s65, v183
	v_med3_f32 v5, v5, s65, v183
	v_pk_add_f32 v[210:211], v[210:211], 1.0 op_sel_hi:[1,0]
	v_pk_add_f32 v[212:213], v[212:213], 1.0 op_sel_hi:[1,0]
	v_pk_add_f32 v[214:215], v[214:215], 1.0 op_sel_hi:[1,0]
	v_pk_add_f32 v[216:217], v[216:217], 1.0 op_sel_hi:[1,0]
	v_pk_add_f32 v[218:219], v[218:219], 1.0 op_sel_hi:[1,0]
	v_pk_add_f32 v[220:221], v[220:221], 1.0 op_sel_hi:[1,0]
	v_pk_add_f32 v[222:223], v[222:223], 1.0 op_sel_hi:[1,0]
	v_pk_add_f32 v[224:225], v[224:225], 1.0 op_sel_hi:[1,0]
	v_rcp_f32_e32 v210, v210
	v_rcp_f32_e32 v211, v211
	v_rcp_f32_e32 v212, v212
	v_rcp_f32_e32 v213, v213
	v_rcp_f32_e32 v214, v214
	v_rcp_f32_e32 v215, v215
	v_rcp_f32_e32 v216, v216
	v_rcp_f32_e32 v217, v217
	v_rcp_f32_e32 v218, v218
	v_rcp_f32_e32 v219, v219
	v_rcp_f32_e32 v220, v220
	v_rcp_f32_e32 v221, v221
	v_rcp_f32_e32 v222, v222
	v_rcp_f32_e32 v223, v223
	v_rcp_f32_e32 v224, v224
	v_rcp_f32_e32 v225, v225
	v_pk_fma_f32 v[14:15], v[14:15], 4.0, 4.0 op_sel_hi:[1,0,0]
	v_pk_fma_f32 v[16:17], v[16:17], 4.0, 4.0 op_sel_hi:[1,0,0]
	v_pk_fma_f32 v[10:11], v[10:11], 4.0, 4.0 op_sel_hi:[1,0,0]
	v_pk_fma_f32 v[12:13], v[12:13], 4.0, 4.0 op_sel_hi:[1,0,0]
	v_pk_fma_f32 v[6:7], v[6:7], 4.0, 4.0 op_sel_hi:[1,0,0]
	v_pk_fma_f32 v[8:9], v[8:9], 4.0, 4.0 op_sel_hi:[1,0,0]
	v_pk_fma_f32 v[2:3], v[2:3], 4.0, 4.0 op_sel_hi:[1,0,0]
	v_pk_fma_f32 v[4:5], v[4:5], 4.0, 4.0 op_sel_hi:[1,0,0]
	v_pk_mul_f32 v[38:39], v[38:39], v[210:211]
	v_pk_mul_f32 v[40:41], v[40:41], v[212:213]
	v_pk_mul_f32 v[34:35], v[34:35], v[214:215]
	v_pk_mul_f32 v[36:37], v[36:37], v[216:217]
	v_pk_mul_f32 v[22:23], v[22:23], v[218:219]
	v_pk_mul_f32 v[24:25], v[24:25], v[220:221]
	v_pk_mul_f32 v[18:19], v[18:19], v[222:223]
	v_pk_mul_f32 v[20:21], v[20:21], v[224:225]
	v_pk_mul_f32 v[38:39], v[38:39], v[14:15]
	v_pk_mul_f32 v[40:41], v[40:41], v[16:17]
	v_pk_mul_f32 v[34:35], v[34:35], v[10:11]
	v_pk_mul_f32 v[36:37], v[36:37], v[12:13]
	v_pk_mul_f32 v[22:23], v[22:23], v[6:7]
	v_pk_mul_f32 v[24:25], v[24:25], v[8:9]
	v_pk_mul_f32 v[18:19], v[18:19], v[2:3]
	v_pk_mul_f32 v[20:21], v[20:21], v[4:5]
	v_cvt_pk_fp8_f32 v140, v38, v39
	v_cvt_pk_fp8_f32 v140, v40, v41 op_sel:[0,0,1]
	v_cvt_pk_fp8_f32 v141, v34, v35
	v_cvt_pk_fp8_f32 v141, v36, v37 op_sel:[0,0,1]
	v_cvt_pk_fp8_f32 v142, v22, v23
	v_cvt_pk_fp8_f32 v142, v24, v25 op_sel:[0,0,1]
	v_cvt_pk_fp8_f32 v143, v18, v19
	v_cvt_pk_fp8_f32 v143, v20, v21 op_sel:[0,0,1]
	v_or_b32_e32 v230, v233, v173
	v_ashrrev_i32_e32 v231, 31, v230
	v_lshlrev_b64 v[230:231], 11, v[230:231]
	v_permlane16_swap_b32_e32 v140, v142
	v_permlane16_swap_b32_e32 v141, v143
	v_lshl_add_u64 v[230:231], s[16:17], 0, v[230:231]
	v_lshl_add_u64 v[230:231], v[230:231], 0, v[130:131]
	global_store_dwordx4 v[230:231], v[140:143], off
	s_and_b64 vcc, exec, s[2:3]
	s_mov_b64 s[0:1], -1
	s_cbranch_vccnz .LBB0_796
	s_andn2_b64 vcc, exec, s[12:13]
	s_cbranch_vccnz .LBB0_795
	s_barrier
	s_branch .LBB0_795

; __global__ void __launch_bounds__(NWAVES * 64, 2) fwd_kernel(Args args) {
;     extern __shared__ __attribute__((aligned(16))) unsigned char lds[];
	.amdhsa_kernel _Z10fwd_kernel4Args
		.amdhsa_group_segment_fixed_size 0
		.amdhsa_private_segment_fixed_size 0
		.amdhsa_kernarg_size 448
		.amdhsa_user_sgpr_count 2
		.amdhsa_user_sgpr_dispatch_ptr 0
		.amdhsa_user_sgpr_queue_ptr 0
		.amdhsa_user_sgpr_kernarg_segment_ptr 1
		.amdhsa_user_sgpr_dispatch_id 0
		.amdhsa_user_sgpr_kernarg_preload_length 0
		.amdhsa_user_sgpr_kernarg_preload_offset 0
		.amdhsa_user_sgpr_private_segment_size 0
		.amdhsa_uses_dynamic_stack 0
		.amdhsa_enable_private_segment 0
		.amdhsa_system_sgpr_workgroup_id_x 1
		.amdhsa_system_sgpr_workgroup_id_y 0
		.amdhsa_system_sgpr_workgroup_id_z 0
		.amdhsa_system_sgpr_workgroup_info 0
		.amdhsa_system_vgpr_workitem_id 0
		.amdhsa_next_free_vgpr 256
		.amdhsa_next_free_sgpr 100
		.amdhsa_accum_offset 256
		.amdhsa_reserve_vcc 1
		.amdhsa_float_round_mode_32 0
		.amdhsa_float_round_mode_16_64 0
		.amdhsa_float_denorm_mode_32 3
		.amdhsa_float_denorm_mode_16_64 3
		.amdhsa_dx10_clamp 1
		.amdhsa_ieee_mode 1
		.amdhsa_fp16_overflow 0
		.amdhsa_tg_split 0
		.amdhsa_exception_fp_ieee_invalid_op 0
		.amdhsa_exception_fp_denorm_src 0
		.amdhsa_exception_fp_ieee_div_zero 0
		.amdhsa_exception_fp_ieee_overflow 0
		.amdhsa_exception_fp_ieee_underflow 0
		.amdhsa_exception_fp_ieee_inexact 0
		.amdhsa_exception_int_div_zero 0
	.end_amdhsa_kernel

; __global__ void __launch_bounds__(NWAVES * 64, 2) fwd_kernel(Args args) {
;     extern __shared__ __attribute__((aligned(16))) unsigned char lds[];
amdhsa.kernels:
  - .agpr_count:     0
    .args:
      - .offset:         0
        .size:           192
        .value_kind:     by_value
      - .offset:         192
        .size:           4
        .value_kind:     hidden_block_count_x
      - .offset:         196
        .size:           4
        .value_kind:     hidden_block_count_y
      - .offset:         200
        .size:           4
        .value_kind:     hidden_block_count_z
      - .offset:         204
        .size:           2
        .value_kind:     hidden_group_size_x
      - .offset:         206
        .size:           2
        .value_kind:     hidden_group_size_y
      - .offset:         208
        .size:           2
        .value_kind:     hidden_group_size_z
      - .offset:         210
        .size:           2
        .value_kind:     hidden_remainder_x
      - .offset:         212
        .size:           2
        .value_kind:     hidden_remainder_y
      - .offset:         214
        .size:           2
        .value_kind:     hidden_remainder_z
      - .offset:         232
        .size:           8
        .value_kind:     hidden_global_offset_x
      - .offset:         240
        .size:           8
        .value_kind:     hidden_global_offset_y
      - .offset:         248
        .size:           8
        .value_kind:     hidden_global_offset_z
      - .offset:         256
        .size:           2
        .value_kind:     hidden_grid_dims
      - .offset:         312
        .size:           4
        .value_kind:     hidden_dynamic_lds_size
    .group_segment_fixed_size: 0
    .kernarg_segment_align: 8
    .kernarg_segment_size: 448
    .language:       OpenCL C
    .language_version:
      - 2
      - 0
    .max_flat_workgroup_size: 512
    .name:           _Z10fwd_kernel4Args
    .private_segment_fixed_size: 0
    .sgpr_count:     106
    .sgpr_spill_count: 108
    .symbol:         _Z10fwd_kernel4Args.kd
    .uniform_work_group_size: 1
    .uses_dynamic_stack: false
    .vgpr_count:     256
    .vgpr_spill_count: 0
    .wavefront_size: 64
